# speedup vs baseline: 1.0050x; 1.0050x over previous
_Z8dog_mainPKfS0_S0_S0_S0_S0_S0_Pf:
	s_nop 0
	s_nop 0
	s_nop 0
	s_nop 0
	s_nop 0
	s_nop 0
	s_nop 0
	s_nop 0
	s_load_dwordx8 s[12:19], s[0:1], 0x0
	s_load_dwordx8 s[20:27], s[0:1], 0x20
	s_and_b32 s3, s2, 7
	s_lshl_b32 s3, s3, 5
	s_lshr_b32 s4, s2, 3
	s_add_i32 s4, s3, s4
	s_and_b32 s6, s4, 3
	s_lshr_b32 s7, s4, 2
	s_mov_b32 s5, 0
	s_lshl_b64 s[8:9], s[4:5], 18
	v_and_b32_e32 v1, 63, v0
	v_lshrrev_b32_e32 v2, 6, v0
	v_and_b32_e32 v3, 31, v0
	v_lshl_or_b32 v4, v2, 5, v3
	v_lshlrev_b32_e32 v5, 2, v4
	v_lshlrev_b32_e32 v6, 4, v1
	v_lshl_or_b32 v6, v2, 12, v6
	s_waitcnt lgkmcnt(0)
	global_load_dword v20, v5, s[18:19]
	global_load_dword v21, v5, s[20:21]
	global_load_dword v22, v5, s[22:23]
	global_load_dword v23, v5, s[24:25]
	global_load_dword v24, v5, s[14:15]
	global_load_dword v25, v5, s[16:17]
	s_add_u32 s12, s12, s8
	s_addc_u32 s13, s13, s9
	global_load_dwordx4 v[128:131], v6, s[12:13] offset:0 nt
	global_load_dwordx4 v[132:135], v6, s[12:13] offset:1024 nt
	global_load_dwordx4 v[136:139], v6, s[12:13] offset:2048 nt
	global_load_dwordx4 v[140:143], v6, s[12:13] offset:3072 nt
	v_add_u32_e32 v6, 0x8000, v6
	global_load_dwordx4 v[144:147], v6, s[12:13] offset:0 nt
	global_load_dwordx4 v[148:151], v6, s[12:13] offset:1024 nt
	global_load_dwordx4 v[152:155], v6, s[12:13] offset:2048 nt
	global_load_dwordx4 v[156:159], v6, s[12:13] offset:3072 nt
	v_bfe_u32 v7, v0, 5, 1
	v_and_b32_e32 v16, 1, v0
	v_cmp_eq_u32_e64 s[30:31], 0, v16
	v_and_b32_e32 v17, 2, v0
	v_cmp_eq_u32_e64 s[32:33], 0, v17
	v_and_b32_e32 v16, 3, v0
	v_lshrrev_b32_e32 v17, 2, v1
	v_lshlrev_b32_e32 v16, 5, v16
	v_lshl_add_u32 v16, v17, 1, v16
	v_lshrrev_b32_e32 v17, 1, v2
	s_movk_i32 s10, 0x110
	v_mad_u32_u24 v16, v17, s10, v16
	v_and_b32_e32 v17, 1, v2
	v_lshl_add_u32 v14, v17, 7, v16
	v_lshlrev_b32_e32 v17, 4, v7
	v_mad_u32_u24 v15, v3, s10, v17
	s_lshl_b32 s11, s6, 5
	v_lshl_add_u32 v18, v7, 2, s11
	v_cvt_f32_u32_e32 v18, v18
	v_lshlrev_b32_e32 v19, 3, v7
	v_cvt_f32_u32_e32 v19, v19
	s_waitcnt vmcnt(8)
	v_add_f32_e32 v26, v20, v21
	v_rcp_f32_e32 v27, v20
	v_rcp_f32_e32 v28, v26
	v_sub_f32_e32 v12, v19, v22
	v_sub_f32_e32 v13, v18, v23
	v_fma_f32 v29, -v20, v27, 1.0
	v_fma_f32 v30, -v26, v28, 1.0
	v_fma_f32 v27, v29, v27, v27
	v_fma_f32 v28, v30, v28, v28
	v_mul_f32_e32 v8, 0xbf38aa3b, v27
	v_mul_f32_e32 v9, 0xbf38aa3b, v28
	v_mul_f32_e32 v29, v24, v27
	v_mul_f32_e32 v30, v25, v28
	v_mul_f32_e32 v10, 0x3e22f983, v29
	v_mul_f32_e32 v11, 0x3e22f983, v30
	s_getpc_b64 s[44:45]
